# v71 plus softmax row max: 7 v_max3 + 1 v_max instead of 3 canonicalising v_max + 7 v_max3 (sel-attn and cmp-attn pass 0)
# speedup vs baseline: 1.0095x; 1.0033x over previous
;     ...
;                         float mx;
;                         { float m = fmaxf(fmaxf(sc[0][0], sc[0][1]), sc[0][2]);
;                           m = fmaxf(fmaxf(m, sc[0][3]), sc[1][0]); m = fmaxf(fmaxf(m, sc[1][1]), sc[1][2]); m = fmaxf(fmaxf(m, sc[1][3]), sc[2][0]);
;                           m = fmaxf(fmaxf(m, sc[2][1]), sc[2][2]); m = fmaxf(fmaxf(m, sc[2][3]), sc[3][0]); m = fmaxf(fmaxf(m, sc[3][1]), sc[3][2]); mx = fmaxf(m, sc[3][3]) + bshift; }
;                         if (MODE == 3 && !colsel) mx = -1e30f;
;                         float p[4][4];
;                         constexpr float L2E = 1.4426950408889634f;
;                         if (MODE == 2 && pass == 1) {
;                             const float negm1 = (mrun[qd] < -1e29f ? 0.f : -mrun[qd] * L2E) + boff + linv[qd];
; #pragma unroll
;                             for (int kt = 0; kt < 4; ++kt)
; #pragma unroll
;                                 for (int r = 0; r < 4; ++r) p[kt][r] = __builtin_amdgcn_exp2f(__builtin_fmaf(sc[kt][r], L2E, negm1));
;                         } else if (MODE == 2) {
;                             const float mn = fmaxf(mrun[qd], mx), corr = __expf(mrun[qd] - mn); mrun[qd] = mn; float ps = 0.f;
;                             const float negm0 = (mn < -1e29f ? 0.f : -mn * L2E) + boff;
; #pragma unroll
;                             for (int kt = 0; kt < 4; ++kt)
; #pragma unroll
;                                 for (int r = 0; r < 4; ++r) ps += __builtin_amdgcn_exp2f(__builtin_fmaf(sc[kt][r], L2E, negm0));
;                             lrun[qd] = lrun[qd] * corr + ps;
.LBB0_890:
	v_max3_f32 v167, v134, v135, v136
	v_max3_f32 v167, v167, v137, v130
	v_max3_f32 v167, v167, v131, v132
	v_max3_f32 v167, v167, v133, v126
	v_max3_f32 v167, v167, v127, v128
	v_max3_f32 v167, v167, v129, v122
	v_max3_f32 v167, v167, v123, v124
	v_max_f32_e32 v167, v167, v125
	v_add_f32_e32 v166, v166, v167
	v_max_f32_e32 v167, v164, v164
	v_max_f32_e32 v166, v167, v166
	v_sub_f32_e32 v167, v164, v166
	v_mul_f32_e32 v167, 0x3fb8aa3b, v167
	v_exp_f32_e32 v192, v167
	v_mul_f32_e32 v167, 0xbfb8aa3b, v166
	v_cmp_ngt_f32_e32 vcc, s30, v166
	s_nop 1
	v_cndmask_b32_e32 v167, 0, v167, vcc
	v_add_f32_e32 v167, v191, v167
	v_fmamk_f32 v193, v134, 0x3fb8aa3b, v167
	v_exp_f32_e32 v193, v193
	v_fmamk_f32 v235, v135, 0x3fb8aa3b, v167
	v_exp_f32_e32 v235, v235
	v_add_f32_e32 v193, 0, v193
	v_add_f32_e32 v193, v235, v193
	v_fmamk_f32 v235, v136, 0x3fb8aa3b, v167
	v_exp_f32_e32 v235, v235
	s_nop 0
	v_add_f32_e32 v193, v235, v193
	v_fmamk_f32 v235, v137, 0x3fb8aa3b, v167
	v_exp_f32_e32 v235, v235
	s_nop 0
	v_add_f32_e32 v193, v235, v193
	v_fmamk_f32 v235, v130, 0x3fb8aa3b, v167
	v_exp_f32_e32 v235, v235
	s_nop 0
	v_add_f32_e32 v193, v235, v193
	v_fmamk_f32 v235, v131, 0x3fb8aa3b, v167
	v_exp_f32_e32 v235, v235
	s_nop 0
	v_add_f32_e32 v193, v235, v193
	v_fmamk_f32 v235, v132, 0x3fb8aa3b, v167
	v_exp_f32_e32 v235, v235
	s_nop 0
	v_add_f32_e32 v193, v235, v193
	v_fmamk_f32 v235, v133, 0x3fb8aa3b, v167
	v_exp_f32_e32 v235, v235
	s_nop 0
	v_add_f32_e32 v193, v235, v193
	v_fmamk_f32 v235, v126, 0x3fb8aa3b, v167
	v_exp_f32_e32 v235, v235
	s_nop 0
	v_add_f32_e32 v193, v235, v193
	v_fmamk_f32 v235, v127, 0x3fb8aa3b, v167
	v_exp_f32_e32 v235, v235
	s_nop 0
	v_add_f32_e32 v193, v235, v193
	v_fmamk_f32 v235, v128, 0x3fb8aa3b, v167
	v_exp_f32_e32 v235, v235
	s_nop 0
	v_add_f32_e32 v193, v235, v193
	v_fmamk_f32 v235, v129, 0x3fb8aa3b, v167
	v_exp_f32_e32 v235, v235
	s_nop 0
	v_add_f32_e32 v193, v235, v193
	v_fmamk_f32 v235, v122, 0x3fb8aa3b, v167
	v_exp_f32_e32 v235, v235
	s_nop 0
	v_add_f32_e32 v193, v235, v193
	v_fmamk_f32 v235, v123, 0x3fb8aa3b, v167
	v_exp_f32_e32 v235, v235
	s_nop 0
	v_add_f32_e32 v193, v235, v193
	v_fmamk_f32 v235, v124, 0x3fb8aa3b, v167
	v_exp_f32_e32 v235, v235
	v_fmac_f32_e32 v167, 0x3fb8aa3b, v125
	v_exp_f32_e32 v167, v167
	v_add_f32_e32 v193, v235, v193
	v_add_f32_e32 v193, v167, v193
	v_fmac_f32_e32 v193, v162, v192
	v_mov_b32_e32 v167, v165
	v_mov_b32_e32 v162, v193
	s_cbranch_execnz .LBB0_892

;     ...
;                         float mx;
;                         { float m = fmaxf(fmaxf(sc[0][0], sc[0][1]), sc[0][2]);
;                           m = fmaxf(fmaxf(m, sc[0][3]), sc[1][0]); m = fmaxf(fmaxf(m, sc[1][1]), sc[1][2]); m = fmaxf(fmaxf(m, sc[1][3]), sc[2][0]);
;                           m = fmaxf(fmaxf(m, sc[2][1]), sc[2][2]); m = fmaxf(fmaxf(m, sc[2][3]), sc[3][0]); m = fmaxf(fmaxf(m, sc[3][1]), sc[3][2]); mx = fmaxf(m, sc[3][3]) + bshift; }
;                         if (MODE == 3 && !colsel) mx = -1e30f;
;                         float p[4][4];
;                         constexpr float L2E = 1.4426950408889634f;
;                         if (MODE == 2 && pass == 1) {
;                             const float negm1 = (mrun[qd] < -1e29f ? 0.f : -mrun[qd] * L2E) + boff + linv[qd];
; #pragma unroll
;                             for (int kt = 0; kt < 4; ++kt)
; #pragma unroll
;                                 for (int r = 0; r < 4; ++r) p[kt][r] = __builtin_amdgcn_exp2f(__builtin_fmaf(sc[kt][r], L2E, negm1));
;                         } else if (MODE == 2) {
;                             const float mn = fmaxf(mrun[qd], mx), corr = __expf(mrun[qd] - mn); mrun[qd] = mn; float ps = 0.f;
;                             const float negm0 = (mn < -1e29f ? 0.f : -mn * L2E) + boff;
; #pragma unroll
;                             for (int kt = 0; kt < 4; ++kt)
; #pragma unroll
;                                 for (int r = 0; r < 4; ++r) ps += __builtin_amdgcn_exp2f(__builtin_fmaf(sc[kt][r], L2E, negm0));
;                             lrun[qd] = lrun[qd] * corr + ps;
.LBB0_906:
	v_max3_f32 v104, v114, v115, v116
	v_max3_f32 v104, v104, v117, v98
	v_max3_f32 v104, v104, v99, v100
	v_max3_f32 v104, v104, v101, v94
	v_max3_f32 v104, v104, v95, v96
	v_max3_f32 v104, v104, v97, v90
	v_max3_f32 v104, v104, v91, v92
	v_max_f32_e32 v104, v104, v93
	v_add_f32_e32 v103, v103, v104
	v_max_f32_e32 v104, v167, v167
	v_max_f32_e32 v165, v104, v103
	v_mul_f32_e32 v104, 0xbfb8aa3b, v165
	v_cmp_ngt_f32_e32 vcc, s30, v165
	v_sub_f32_e32 v103, v167, v165
	v_mul_f32_e32 v103, 0x3fb8aa3b, v103
	v_cndmask_b32_e32 v104, 0, v104, vcc
	v_add_f32_e32 v104, v102, v104
	v_fmamk_f32 v105, v114, 0x3fb8aa3b, v104
	v_exp_f32_e32 v105, v105
	v_fmamk_f32 v106, v115, 0x3fb8aa3b, v104
	v_exp_f32_e32 v106, v106
	v_exp_f32_e32 v103, v103
	v_add_f32_e32 v105, 0, v105
	v_mov_b32_e32 v164, v166
	v_add_f32_e32 v105, v106, v105
	v_fmamk_f32 v106, v116, 0x3fb8aa3b, v104
	v_exp_f32_e32 v106, v106
	s_nop 0
	v_add_f32_e32 v105, v106, v105
	v_fmamk_f32 v106, v117, 0x3fb8aa3b, v104
	v_exp_f32_e32 v106, v106
	s_nop 0
	v_add_f32_e32 v105, v106, v105
	v_fmamk_f32 v106, v98, 0x3fb8aa3b, v104
	v_exp_f32_e32 v106, v106
	s_nop 0
	v_add_f32_e32 v105, v106, v105
	v_fmamk_f32 v106, v99, 0x3fb8aa3b, v104
	v_exp_f32_e32 v106, v106
	s_nop 0
	v_add_f32_e32 v105, v106, v105
	v_fmamk_f32 v106, v100, 0x3fb8aa3b, v104
	v_exp_f32_e32 v106, v106
	s_nop 0
	v_add_f32_e32 v105, v106, v105
	v_fmamk_f32 v106, v101, 0x3fb8aa3b, v104
	v_exp_f32_e32 v106, v106
	s_nop 0
	v_add_f32_e32 v105, v106, v105
	v_fmamk_f32 v106, v94, 0x3fb8aa3b, v104
	v_exp_f32_e32 v106, v106
	s_nop 0
	v_add_f32_e32 v105, v106, v105
	v_fmamk_f32 v106, v95, 0x3fb8aa3b, v104
	v_exp_f32_e32 v106, v106
	s_nop 0
	v_add_f32_e32 v105, v106, v105
	v_fmamk_f32 v106, v96, 0x3fb8aa3b, v104
	v_exp_f32_e32 v106, v106
	s_nop 0
	v_add_f32_e32 v105, v106, v105
	v_fmamk_f32 v106, v97, 0x3fb8aa3b, v104
	v_exp_f32_e32 v106, v106
	s_nop 0
	v_add_f32_e32 v105, v106, v105
	v_fmamk_f32 v106, v90, 0x3fb8aa3b, v104
	v_exp_f32_e32 v106, v106
	s_nop 0
	v_add_f32_e32 v105, v106, v105
	v_fmamk_f32 v106, v91, 0x3fb8aa3b, v104
	v_exp_f32_e32 v106, v106
	s_nop 0
	v_add_f32_e32 v105, v106, v105
	v_fmamk_f32 v106, v92, 0x3fb8aa3b, v104
	v_exp_f32_e32 v106, v106
	v_fmac_f32_e32 v104, 0x3fb8aa3b, v93
	v_exp_f32_e32 v104, v104
	v_add_f32_e32 v105, v106, v105
	v_add_f32_e32 v104, v104, v105
	v_fmac_f32_e32 v104, v163, v103
	v_mov_b32_e32 v163, v104
	s_cbranch_execnz .LBB0_908

;     ...
;                         float mx;
;                         { float m = fmaxf(fmaxf(sc[0][0], sc[0][1]), sc[0][2]);
;                           m = fmaxf(fmaxf(m, sc[0][3]), sc[1][0]); m = fmaxf(fmaxf(m, sc[1][1]), sc[1][2]); m = fmaxf(fmaxf(m, sc[1][3]), sc[2][0]);
;                           m = fmaxf(fmaxf(m, sc[2][1]), sc[2][2]); m = fmaxf(fmaxf(m, sc[2][3]), sc[3][0]); m = fmaxf(fmaxf(m, sc[3][1]), sc[3][2]); mx = fmaxf(m, sc[3][3]) + bshift; }
;                         if (MODE == 3 && !colsel) mx = -1e30f;
;                         float p[4][4];
;                         constexpr float L2E = 1.4426950408889634f;
;                         if (MODE == 2 && pass == 1) {
;                             const float negm1 = (mrun[qd] < -1e29f ? 0.f : -mrun[qd] * L2E) + boff + linv[qd];
; #pragma unroll
;                             for (int kt = 0; kt < 4; ++kt)
; #pragma unroll
;                                 for (int r = 0; r < 4; ++r) p[kt][r] = __builtin_amdgcn_exp2f(__builtin_fmaf(sc[kt][r], L2E, negm1));
;                         } else if (MODE == 2) {
;                             const float mn = fmaxf(mrun[qd], mx), corr = __expf(mrun[qd] - mn); mrun[qd] = mn; float ps = 0.f;
;                             const float negm0 = (mn < -1e29f ? 0.f : -mn * L2E) + boff;
; #pragma unroll
;                             for (int kt = 0; kt < 4; ++kt)
; #pragma unroll
;                                 for (int r = 0; r < 4; ++r) ps += __builtin_amdgcn_exp2f(__builtin_fmaf(sc[kt][r], L2E, negm0));
;                             lrun[qd] = lrun[qd] * corr + ps;
;                         } else {
;                             if (__any(mx > mrun[qd] + 6.0f)) {
;                                 mx = fmaxf(mx, __shfl_xor(mx, 16)); mx = fmaxf(mx, __shfl_xor(mx, 32));
;                                 const float mn = fmaxf(mrun[qd], mx), corr = __expf(mrun[qd] - mn); mrun[qd] = mn;
;                                 lrun[qd] *= corr;
; #pragma unroll
;                                 for (int dt = 0; dt < 4; ++dt) O[qd][dt] = O[qd][dt] * corr;
;                             }
.LBB0_1163:
	v_and_b32_e32 v192, s0, v191
	v_cmp_eq_u32_e64 s[4:5], 0, v192
	v_max3_f32 v192, v150, v151, v152
	v_max3_f32 v192, v192, v153, v146
	v_max3_f32 v192, v192, v147, v148
	v_max3_f32 v192, v192, v149, v142
	v_max3_f32 v192, v192, v143, v144
	v_max3_f32 v192, v192, v145, v110
	v_max3_f32 v192, v192, v111, v112
	v_max_f32_e32 v192, v192, v113
	v_add_f32_e32 v192, v237, v192
	v_cndmask_b32_e64 v192, v192, v190, s[4:5]
	v_add_f32_e32 v193, 0x40c00000, v167
	v_cmp_gt_f32_e32 vcc, v192, v193
	s_cbranch_vccz .LBB0_1165
	ds_bpermute_b32 v193, v230, v192
	v_max_f32_e32 v192, v192, v192
	s_waitcnt lgkmcnt(0)
	v_max_f32_e32 v193, v193, v193
	v_max_f32_e32 v192, v192, v193
	ds_bpermute_b32 v193, v231, v192
	s_waitcnt lgkmcnt(0)
	v_max3_f32 v193, v167, v192, v193
	v_sub_f32_e32 v167, v167, v193
	v_mul_f32_e32 v167, 0x3fb8aa3b, v167
	v_exp_f32_e32 v192, v167
	v_mov_b32_e32 v167, v193
	v_mul_f32_e32 v203, v203, v192
	v_pk_mul_f32 v[104:105], v[104:105], v[192:193] op_sel_hi:[1,0]
	v_pk_mul_f32 v[102:103], v[102:103], v[192:193] op_sel_hi:[1,0]
	v_pk_mul_f32 v[100:101], v[100:101], v[192:193] op_sel_hi:[1,0]
	v_pk_mul_f32 v[98:99], v[98:99], v[192:193] op_sel_hi:[1,0]
	v_pk_mul_f32 v[96:97], v[96:97], v[192:193] op_sel_hi:[1,0]
	v_pk_mul_f32 v[94:95], v[94:95], v[192:193] op_sel_hi:[1,0]
	v_pk_mul_f32 v[92:93], v[92:93], v[192:193] op_sel_hi:[1,0]
	v_pk_mul_f32 v[90:91], v[90:91], v[192:193] op_sel_hi:[1,0]

;     ...
;                         float mx;
;                         { float m = fmaxf(fmaxf(sc[0][0], sc[0][1]), sc[0][2]);
;                           m = fmaxf(fmaxf(m, sc[0][3]), sc[1][0]); m = fmaxf(fmaxf(m, sc[1][1]), sc[1][2]); m = fmaxf(fmaxf(m, sc[1][3]), sc[2][0]);
;                           m = fmaxf(fmaxf(m, sc[2][1]), sc[2][2]); m = fmaxf(fmaxf(m, sc[2][3]), sc[3][0]); m = fmaxf(fmaxf(m, sc[3][1]), sc[3][2]); mx = fmaxf(m, sc[3][3]) + bshift; }
;                         if (MODE == 3 && !colsel) mx = -1e30f;
;                         float p[4][4];
;                         constexpr float L2E = 1.4426950408889634f;
;                         if (MODE == 2 && pass == 1) {
;                             const float negm1 = (mrun[qd] < -1e29f ? 0.f : -mrun[qd] * L2E) + boff + linv[qd];
; #pragma unroll
;                             for (int kt = 0; kt < 4; ++kt)
; #pragma unroll
;                                 for (int r = 0; r < 4; ++r) p[kt][r] = __builtin_amdgcn_exp2f(__builtin_fmaf(sc[kt][r], L2E, negm1));
;                         } else if (MODE == 2) {
;                             const float mn = fmaxf(mrun[qd], mx), corr = __expf(mrun[qd] - mn); mrun[qd] = mn; float ps = 0.f;
;                             const float negm0 = (mn < -1e29f ? 0.f : -mn * L2E) + boff;
; #pragma unroll
;                             for (int kt = 0; kt < 4; ++kt)
; #pragma unroll
;                                 for (int r = 0; r < 4; ++r) ps += __builtin_amdgcn_exp2f(__builtin_fmaf(sc[kt][r], L2E, negm0));
;                             lrun[qd] = lrun[qd] * corr + ps;
;                         } else {
;                             if (__any(mx > mrun[qd] + 6.0f)) {
;                                 mx = fmaxf(mx, __shfl_xor(mx, 16)); mx = fmaxf(mx, __shfl_xor(mx, 32));
;                                 const float mn = fmaxf(mrun[qd], mx), corr = __expf(mrun[qd] - mn); mrun[qd] = mn;
;                                 lrun[qd] *= corr;
; #pragma unroll
;                                 for (int dt = 0; dt < 4; ++dt) O[qd][dt] = O[qd][dt] * corr;
;                             }
.LBB0_1172:
	v_and_b32_e32 v192, s0, v205
	v_cmp_eq_u32_e64 s[0:1], 0, v192
	v_max3_f32 v192, v150, v151, v152
	v_max3_f32 v192, v192, v153, v146
	v_max3_f32 v192, v192, v147, v148
	v_max3_f32 v192, v192, v149, v142
	v_max3_f32 v192, v192, v143, v144
	v_max3_f32 v192, v192, v145, v110
	v_max3_f32 v192, v192, v111, v112
	v_max_f32_e32 v192, v192, v113
	v_add_f32_e32 v192, v237, v192
	v_cndmask_b32_e64 v192, v192, v190, s[0:1]
	v_add_f32_e32 v193, 0x40c00000, v236
	v_cmp_gt_f32_e32 vcc, v192, v193
	s_cbranch_vccz .LBB0_1174
	ds_bpermute_b32 v193, v230, v192
	v_max_f32_e32 v192, v192, v192
	s_waitcnt lgkmcnt(0)
	v_max_f32_e32 v193, v193, v193
	v_max_f32_e32 v192, v192, v193
	ds_bpermute_b32 v193, v231, v192
	s_waitcnt lgkmcnt(0)
	v_max3_f32 v193, v236, v192, v193
	v_sub_f32_e32 v192, v236, v193
	v_mul_f32_e32 v192, 0x3fb8aa3b, v192
	v_exp_f32_e32 v192, v192
	v_mov_b32_e32 v236, v193
	v_mul_f32_e32 v202, v202, v192
	v_pk_mul_f32 v[88:89], v[88:89], v[192:193] op_sel_hi:[1,0]
	v_pk_mul_f32 v[86:87], v[86:87], v[192:193] op_sel_hi:[1,0]
	v_pk_mul_f32 v[84:85], v[84:85], v[192:193] op_sel_hi:[1,0]
	v_pk_mul_f32 v[82:83], v[82:83], v[192:193] op_sel_hi:[1,0]
	v_pk_mul_f32 v[80:81], v[80:81], v[192:193] op_sel_hi:[1,0]
	v_pk_mul_f32 v[78:79], v[78:79], v[192:193] op_sel_hi:[1,0]
	v_pk_mul_f32 v[76:77], v[76:77], v[192:193] op_sel_hi:[1,0]
	v_pk_mul_f32 v[74:75], v[74:75], v[192:193] op_sel_hi:[1,0]

;     ...
;                         float mx;
;                         { float m = fmaxf(fmaxf(sc[0][0], sc[0][1]), sc[0][2]);
;                           m = fmaxf(fmaxf(m, sc[0][3]), sc[1][0]); m = fmaxf(fmaxf(m, sc[1][1]), sc[1][2]); m = fmaxf(fmaxf(m, sc[1][3]), sc[2][0]);
;                           m = fmaxf(fmaxf(m, sc[2][1]), sc[2][2]); m = fmaxf(fmaxf(m, sc[2][3]), sc[3][0]); m = fmaxf(fmaxf(m, sc[3][1]), sc[3][2]); mx = fmaxf(m, sc[3][3]) + bshift; }
;                         if (MODE == 3 && !colsel) mx = -1e30f;
;                         float p[4][4];
;                         constexpr float L2E = 1.4426950408889634f;
;                         if (MODE == 2 && pass == 1) {
;                             const float negm1 = (mrun[qd] < -1e29f ? 0.f : -mrun[qd] * L2E) + boff + linv[qd];
; #pragma unroll
;                             for (int kt = 0; kt < 4; ++kt)
; #pragma unroll
;                                 for (int r = 0; r < 4; ++r) p[kt][r] = __builtin_amdgcn_exp2f(__builtin_fmaf(sc[kt][r], L2E, negm1));
;                         } else if (MODE == 2) {
;                             const float mn = fmaxf(mrun[qd], mx), corr = __expf(mrun[qd] - mn); mrun[qd] = mn; float ps = 0.f;
;                             const float negm0 = (mn < -1e29f ? 0.f : -mn * L2E) + boff;
; #pragma unroll
;                             for (int kt = 0; kt < 4; ++kt)
; #pragma unroll
;                                 for (int r = 0; r < 4; ++r) ps += __builtin_amdgcn_exp2f(__builtin_fmaf(sc[kt][r], L2E, negm0));
;                             lrun[qd] = lrun[qd] * corr + ps;
;                         } else {
;                             if (__any(mx > mrun[qd] + 6.0f)) {
;                                 mx = fmaxf(mx, __shfl_xor(mx, 16)); mx = fmaxf(mx, __shfl_xor(mx, 32));
;                                 const float mn = fmaxf(mrun[qd], mx), corr = __expf(mrun[qd] - mn); mrun[qd] = mn;
;                                 lrun[qd] *= corr;
; #pragma unroll
;                                 for (int dt = 0; dt < 4; ++dt) O[qd][dt] = O[qd][dt] * corr;
;                             }
.LBB0_1229:
	v_and_b32_e32 v192, s0, v191
	v_cmp_eq_u32_e64 s[4:5], 0, v192
	v_max3_f32 v192, v150, v151, v152
	v_max3_f32 v192, v192, v153, v146
	v_max3_f32 v192, v192, v147, v148
	v_max3_f32 v192, v192, v149, v142
	v_max3_f32 v192, v192, v143, v144
	v_max3_f32 v192, v192, v145, v110
	v_max3_f32 v192, v192, v111, v112
	v_max_f32_e32 v192, v192, v113
	v_add_f32_e32 v192, v239, v192
	v_cndmask_b32_e64 v192, v192, v190, s[4:5]
	v_add_f32_e32 v193, 0x40c00000, v167
	v_cmp_gt_f32_e32 vcc, v192, v193
	s_cbranch_vccz .LBB0_1231
	ds_bpermute_b32 v193, v230, v192
	v_max_f32_e32 v192, v192, v192
	s_waitcnt lgkmcnt(0)
	v_max_f32_e32 v193, v193, v193
	v_max_f32_e32 v192, v192, v193
	ds_bpermute_b32 v193, v231, v192
	s_waitcnt lgkmcnt(0)
	v_max3_f32 v193, v167, v192, v193
	v_sub_f32_e32 v167, v167, v193
	v_mul_f32_e32 v167, 0x3fb8aa3b, v167
	v_exp_f32_e32 v192, v167
	v_mov_b32_e32 v167, v193
	v_mul_f32_e32 v203, v203, v192
	v_pk_mul_f32 v[104:105], v[104:105], v[192:193] op_sel_hi:[1,0]
	v_pk_mul_f32 v[102:103], v[102:103], v[192:193] op_sel_hi:[1,0]
	v_pk_mul_f32 v[100:101], v[100:101], v[192:193] op_sel_hi:[1,0]
	v_pk_mul_f32 v[98:99], v[98:99], v[192:193] op_sel_hi:[1,0]
	v_pk_mul_f32 v[96:97], v[96:97], v[192:193] op_sel_hi:[1,0]
	v_pk_mul_f32 v[94:95], v[94:95], v[192:193] op_sel_hi:[1,0]
	v_pk_mul_f32 v[92:93], v[92:93], v[192:193] op_sel_hi:[1,0]
	v_pk_mul_f32 v[90:91], v[90:91], v[192:193] op_sel_hi:[1,0]

;     ...
;                         float mx;
;                         { float m = fmaxf(fmaxf(sc[0][0], sc[0][1]), sc[0][2]);
;                           m = fmaxf(fmaxf(m, sc[0][3]), sc[1][0]); m = fmaxf(fmaxf(m, sc[1][1]), sc[1][2]); m = fmaxf(fmaxf(m, sc[1][3]), sc[2][0]);
;                           m = fmaxf(fmaxf(m, sc[2][1]), sc[2][2]); m = fmaxf(fmaxf(m, sc[2][3]), sc[3][0]); m = fmaxf(fmaxf(m, sc[3][1]), sc[3][2]); mx = fmaxf(m, sc[3][3]) + bshift; }
;                         if (MODE == 3 && !colsel) mx = -1e30f;
;                         float p[4][4];
;                         constexpr float L2E = 1.4426950408889634f;
;                         if (MODE == 2 && pass == 1) {
;                             const float negm1 = (mrun[qd] < -1e29f ? 0.f : -mrun[qd] * L2E) + boff + linv[qd];
; #pragma unroll
;                             for (int kt = 0; kt < 4; ++kt)
; #pragma unroll
;                                 for (int r = 0; r < 4; ++r) p[kt][r] = __builtin_amdgcn_exp2f(__builtin_fmaf(sc[kt][r], L2E, negm1));
;                         } else if (MODE == 2) {
;                             const float mn = fmaxf(mrun[qd], mx), corr = __expf(mrun[qd] - mn); mrun[qd] = mn; float ps = 0.f;
;                             const float negm0 = (mn < -1e29f ? 0.f : -mn * L2E) + boff;
; #pragma unroll
;                             for (int kt = 0; kt < 4; ++kt)
; #pragma unroll
;                                 for (int r = 0; r < 4; ++r) ps += __builtin_amdgcn_exp2f(__builtin_fmaf(sc[kt][r], L2E, negm0));
;                             lrun[qd] = lrun[qd] * corr + ps;
;                         } else {
;                             if (__any(mx > mrun[qd] + 6.0f)) {
;                                 mx = fmaxf(mx, __shfl_xor(mx, 16)); mx = fmaxf(mx, __shfl_xor(mx, 32));
;                                 const float mn = fmaxf(mrun[qd], mx), corr = __expf(mrun[qd] - mn); mrun[qd] = mn;
;                                 lrun[qd] *= corr;
; #pragma unroll
;                                 for (int dt = 0; dt < 4; ++dt) O[qd][dt] = O[qd][dt] * corr;
;                             }
.LBB0_1251:
	v_and_b32_e32 v192, s0, v191
	v_cmp_eq_u32_e64 s[4:5], 0, v192
	v_max3_f32 v192, v150, v151, v152
	v_max3_f32 v192, v192, v153, v146
	v_max3_f32 v192, v192, v147, v148
	v_max3_f32 v192, v192, v149, v142
	v_max3_f32 v192, v192, v143, v144
	v_max3_f32 v192, v192, v145, v106
	v_max3_f32 v192, v192, v107, v108
	v_max_f32_e32 v192, v192, v109
	v_add_f32_e32 v192, v248, v192
	v_cndmask_b32_e64 v192, v192, v190, s[4:5]
	v_add_f32_e32 v193, 0x40c00000, v167
	v_cmp_gt_f32_e32 vcc, v192, v193
	s_cbranch_vccz .LBB0_1253
	ds_bpermute_b32 v193, v230, v192
	v_max_f32_e32 v192, v192, v192
	s_waitcnt lgkmcnt(0)
	v_max_f32_e32 v193, v193, v193
	v_max_f32_e32 v192, v192, v193
	ds_bpermute_b32 v193, v231, v192
	s_waitcnt lgkmcnt(0)
	v_max3_f32 v193, v167, v192, v193
	v_sub_f32_e32 v167, v167, v193
	v_mul_f32_e32 v167, 0x3fb8aa3b, v167
	v_exp_f32_e32 v192, v167
	v_mov_b32_e32 v167, v193
	v_mul_f32_e32 v203, v203, v192
	v_pk_mul_f32 v[104:105], v[104:105], v[192:193] op_sel_hi:[1,0]
	v_pk_mul_f32 v[102:103], v[102:103], v[192:193] op_sel_hi:[1,0]
	v_pk_mul_f32 v[100:101], v[100:101], v[192:193] op_sel_hi:[1,0]
	v_pk_mul_f32 v[98:99], v[98:99], v[192:193] op_sel_hi:[1,0]
	v_pk_mul_f32 v[96:97], v[96:97], v[192:193] op_sel_hi:[1,0]
	v_pk_mul_f32 v[94:95], v[94:95], v[192:193] op_sel_hi:[1,0]
	v_pk_mul_f32 v[92:93], v[92:93], v[192:193] op_sel_hi:[1,0]
	v_pk_mul_f32 v[90:91], v[90:91], v[192:193] op_sel_hi:[1,0]

;     ...
;                         float mx;
;                         { float m = fmaxf(fmaxf(sc[0][0], sc[0][1]), sc[0][2]);
;                           m = fmaxf(fmaxf(m, sc[0][3]), sc[1][0]); m = fmaxf(fmaxf(m, sc[1][1]), sc[1][2]); m = fmaxf(fmaxf(m, sc[1][3]), sc[2][0]);
;                           m = fmaxf(fmaxf(m, sc[2][1]), sc[2][2]); m = fmaxf(fmaxf(m, sc[2][3]), sc[3][0]); m = fmaxf(fmaxf(m, sc[3][1]), sc[3][2]); mx = fmaxf(m, sc[3][3]) + bshift; }
;                         if (MODE == 3 && !colsel) mx = -1e30f;
;                         float p[4][4];
;                         constexpr float L2E = 1.4426950408889634f;
;                         if (MODE == 2 && pass == 1) {
;                             const float negm1 = (mrun[qd] < -1e29f ? 0.f : -mrun[qd] * L2E) + boff + linv[qd];
; #pragma unroll
;                             for (int kt = 0; kt < 4; ++kt)
; #pragma unroll
;                                 for (int r = 0; r < 4; ++r) p[kt][r] = __builtin_amdgcn_exp2f(__builtin_fmaf(sc[kt][r], L2E, negm1));
;                         } else if (MODE == 2) {
;                             const float mn = fmaxf(mrun[qd], mx), corr = __expf(mrun[qd] - mn); mrun[qd] = mn; float ps = 0.f;
;                             const float negm0 = (mn < -1e29f ? 0.f : -mn * L2E) + boff;
; #pragma unroll
;                             for (int kt = 0; kt < 4; ++kt)
; #pragma unroll
;                                 for (int r = 0; r < 4; ++r) ps += __builtin_amdgcn_exp2f(__builtin_fmaf(sc[kt][r], L2E, negm0));
;                             lrun[qd] = lrun[qd] * corr + ps;
;                         } else {
;                             if (__any(mx > mrun[qd] + 6.0f)) {
;                                 mx = fmaxf(mx, __shfl_xor(mx, 16)); mx = fmaxf(mx, __shfl_xor(mx, 32));
;                                 const float mn = fmaxf(mrun[qd], mx), corr = __expf(mrun[qd] - mn); mrun[qd] = mn;
;                                 lrun[qd] *= corr;
; #pragma unroll
;                                 for (int dt = 0; dt < 4; ++dt) O[qd][dt] = O[qd][dt] * corr;
;                             }
.LBB0_1260:
	v_and_b32_e32 v192, s0, v205
	v_cmp_eq_u32_e64 s[0:1], 0, v192
	v_max3_f32 v192, v150, v151, v152
	v_max3_f32 v192, v192, v153, v146
	v_max3_f32 v192, v192, v147, v148
	v_max3_f32 v192, v192, v149, v142
	v_max3_f32 v192, v192, v143, v144
	v_max3_f32 v192, v192, v145, v106
	v_max3_f32 v192, v192, v107, v108
	v_max_f32_e32 v192, v192, v109
	v_add_f32_e32 v192, v237, v192
	v_cndmask_b32_e64 v192, v192, v190, s[0:1]
	v_add_f32_e32 v193, 0x40c00000, v236
	v_cmp_gt_f32_e32 vcc, v192, v193
	s_cbranch_vccz .LBB0_1262
	ds_bpermute_b32 v193, v230, v192
	v_max_f32_e32 v192, v192, v192
	s_waitcnt lgkmcnt(0)
	v_max_f32_e32 v193, v193, v193
	v_max_f32_e32 v192, v192, v193
	ds_bpermute_b32 v193, v231, v192
	s_waitcnt lgkmcnt(0)
	v_max3_f32 v193, v236, v192, v193
	v_sub_f32_e32 v192, v236, v193
	v_mul_f32_e32 v192, 0x3fb8aa3b, v192
	v_exp_f32_e32 v192, v192
	v_mov_b32_e32 v236, v193
	v_mul_f32_e32 v202, v202, v192
	v_pk_mul_f32 v[88:89], v[88:89], v[192:193] op_sel_hi:[1,0]
	v_pk_mul_f32 v[86:87], v[86:87], v[192:193] op_sel_hi:[1,0]
	v_pk_mul_f32 v[84:85], v[84:85], v[192:193] op_sel_hi:[1,0]
	v_pk_mul_f32 v[82:83], v[82:83], v[192:193] op_sel_hi:[1,0]
	v_pk_mul_f32 v[80:81], v[80:81], v[192:193] op_sel_hi:[1,0]
	v_pk_mul_f32 v[78:79], v[78:79], v[192:193] op_sel_hi:[1,0]
	v_pk_mul_f32 v[76:77], v[76:77], v[192:193] op_sel_hi:[1,0]
	v_pk_mul_f32 v[74:75], v[74:75], v[192:193] op_sel_hi:[1,0]
